# LN0: the xor-1/2/4/8 steps of the 18 per-row wave reductions use DPP moves (quad_perm / row_half_mirror / row_mirror) instead of ds_bpermute LDS round trips; lgkmcnt waits re-counted
# speedup vs baseline: 1.0064x; 1.0064x over previous
.LBB0_1237:
	v_lshlrev_b32_e32 v162, 16, v60
	v_and_b32_e32 v163, 0xffff0000, v60
	v_lshlrev_b32_e32 v164, 16, v56
	v_and_b32_e32 v165, 0xffff0000, v56
	v_lshlrev_b32_e32 v60, 16, v61
	v_and_b32_e32 v61, 0xffff0000, v61
	v_lshlrev_b32_e32 v56, 16, v57
	v_and_b32_e32 v57, 0xffff0000, v57
	v_pk_fma_f32 v[164:165], v[162:163], s[20:21], v[164:165] op_sel_hi:[1,0,1]
	v_pk_fma_f32 v[56:57], v[60:61], s[20:21], v[56:57] op_sel_hi:[1,0,1]
	v_lshlrev_b32_e32 v60, 16, v62
	v_and_b32_e32 v61, 0xffff0000, v62
	v_lshlrev_b32_e32 v162, 16, v58
	v_and_b32_e32 v163, 0xffff0000, v58
	v_pk_fma_f32 v[166:167], v[60:61], s[20:21], v[162:163] op_sel_hi:[1,0,1]
	v_lshlrev_b32_e32 v60, 16, v63
	v_and_b32_e32 v61, 0xffff0000, v63
	v_lshlrev_b32_e32 v58, 16, v59
	v_and_b32_e32 v59, 0xffff0000, v59
	v_pk_fma_f32 v[58:59], v[60:61], s[20:21], v[58:59] op_sel_hi:[1,0,1]
	v_lshlrev_b32_e32 v60, 16, v52
	v_and_b32_e32 v61, 0xffff0000, v52
	v_lshlrev_b32_e32 v62, 16, v48
	v_and_b32_e32 v63, 0xffff0000, v48
	v_lshlrev_b32_e32 v52, 16, v53
	v_and_b32_e32 v53, 0xffff0000, v53
	v_lshlrev_b32_e32 v48, 16, v49
	v_and_b32_e32 v49, 0xffff0000, v49
	v_pk_fma_f32 v[168:169], v[60:61], s[20:21], v[62:63] op_sel_hi:[1,0,1]
	v_pk_fma_f32 v[48:49], v[52:53], s[20:21], v[48:49] op_sel_hi:[1,0,1]
	v_lshlrev_b32_e32 v52, 16, v54
	v_and_b32_e32 v53, 0xffff0000, v54
	v_lshlrev_b32_e32 v60, 16, v50
	v_and_b32_e32 v61, 0xffff0000, v50
	v_lshlrev_b32_e32 v54, 16, v55
	v_and_b32_e32 v55, 0xffff0000, v55
	v_lshlrev_b32_e32 v50, 16, v51
	v_and_b32_e32 v51, 0xffff0000, v51
	v_pk_fma_f32 v[52:53], v[52:53], s[20:21], v[60:61] op_sel_hi:[1,0,1]
	v_pk_fma_f32 v[50:51], v[54:55], s[20:21], v[50:51] op_sel_hi:[1,0,1]
	v_lshlrev_b32_e32 v54, 16, v44
	v_and_b32_e32 v55, 0xffff0000, v44
	v_lshlrev_b32_e32 v60, 16, v40
	v_and_b32_e32 v61, 0xffff0000, v40
	v_lshlrev_b32_e32 v44, 16, v45
	v_and_b32_e32 v45, 0xffff0000, v45
	v_lshlrev_b32_e32 v40, 16, v41
	v_and_b32_e32 v41, 0xffff0000, v41
	v_pk_fma_f32 v[54:55], v[54:55], s[20:21], v[60:61] op_sel_hi:[1,0,1]
	v_pk_fma_f32 v[40:41], v[44:45], s[20:21], v[40:41] op_sel_hi:[1,0,1]
	v_lshlrev_b32_e32 v44, 16, v46
	v_and_b32_e32 v45, 0xffff0000, v46
	v_lshlrev_b32_e32 v60, 16, v42
	v_and_b32_e32 v61, 0xffff0000, v42
	v_lshlrev_b32_e32 v46, 16, v47
	v_and_b32_e32 v47, 0xffff0000, v47
	v_lshlrev_b32_e32 v42, 16, v43
	v_and_b32_e32 v43, 0xffff0000, v43
	v_pk_fma_f32 v[44:45], v[44:45], s[20:21], v[60:61] op_sel_hi:[1,0,1]
	v_pk_fma_f32 v[42:43], v[46:47], s[20:21], v[42:43] op_sel_hi:[1,0,1]
	v_lshlrev_b32_e32 v46, 16, v36
	v_and_b32_e32 v47, 0xffff0000, v36
	v_lshlrev_b32_e32 v60, 16, v32
	v_and_b32_e32 v61, 0xffff0000, v32
	v_lshlrev_b32_e32 v36, 16, v37
	v_and_b32_e32 v37, 0xffff0000, v37
	v_lshlrev_b32_e32 v32, 16, v33
	v_and_b32_e32 v33, 0xffff0000, v33
	v_pk_fma_f32 v[46:47], v[46:47], s[20:21], v[60:61] op_sel_hi:[1,0,1]
	v_pk_fma_f32 v[32:33], v[36:37], s[20:21], v[32:33] op_sel_hi:[1,0,1]
	v_lshlrev_b32_e32 v36, 16, v38
	v_and_b32_e32 v37, 0xffff0000, v38
	v_lshlrev_b32_e32 v60, 16, v34
	v_and_b32_e32 v61, 0xffff0000, v34
	v_lshlrev_b32_e32 v38, 16, v39
	v_and_b32_e32 v39, 0xffff0000, v39
	v_lshlrev_b32_e32 v34, 16, v35
	v_and_b32_e32 v35, 0xffff0000, v35
	v_pk_fma_f32 v[34:35], v[38:39], s[20:21], v[34:35] op_sel_hi:[1,0,1]
	v_add_f32_e32 v38, 0, v164
	v_add_f32_e32 v38, v165, v38
	v_add_f32_e32 v38, v56, v38
	v_add_f32_e32 v38, v57, v38
	v_add_f32_e32 v38, v166, v38
	v_add_f32_e32 v38, v167, v38
	v_add_f32_e32 v38, v58, v38
	v_add_f32_e32 v38, v59, v38
	v_add_f32_e32 v38, v168, v38
	v_add_f32_e32 v38, v169, v38
	v_add_f32_e32 v38, v48, v38
	v_add_f32_e32 v38, v49, v38
	v_add_f32_e32 v38, v52, v38
	v_add_f32_e32 v38, v53, v38
	v_add_f32_e32 v38, v50, v38
	v_add_f32_e32 v38, v51, v38
	v_add_f32_e32 v38, v54, v38
	v_add_f32_e32 v38, v55, v38
	v_add_f32_e32 v38, v40, v38
	v_add_f32_e32 v38, v41, v38
	v_add_f32_e32 v38, v44, v38
	v_add_f32_e32 v38, v45, v38
	v_add_f32_e32 v38, v42, v38
	v_add_f32_e32 v38, v43, v38
	v_add_f32_e32 v38, v46, v38
	v_add_f32_e32 v38, v47, v38
	v_add_f32_e32 v38, v32, v38
	v_pk_fma_f32 v[36:37], v[36:37], s[20:21], v[60:61] op_sel_hi:[1,0,1]
	v_add_f32_e32 v38, v33, v38
	v_and_b32_e32 v39, 64, v195
	v_add_f32_e32 v38, v36, v38
	v_add_u32_e32 v39, 64, v39
	v_xor_b32_e32 v60, 1, v195
	v_add_f32_e32 v38, v37, v38
	v_cmp_lt_i32_e32 vcc, v60, v39
	v_add_f32_e32 v38, v34, v38
	v_add_f32_e32 v38, v35, v38
	v_cndmask_b32_e32 v60, v195, v60, vcc
	v_lshlrev_b32_e32 v60, 2, v60
	s_nop 1
	v_mov_b32_dpp v61, v38 quad_perm:[1,0,3,2] row_mask:0xf bank_mask:0xf
	s_ashr_i32 s7, s6, 31
	s_waitcnt lgkmcnt(0)
	v_add_f32_e32 v38, v38, v61
	v_xor_b32_e32 v61, 2, v195
	v_cmp_lt_i32_e32 vcc, v61, v39
	s_nop 1
	v_cndmask_b32_e32 v61, v195, v61, vcc
	v_lshlrev_b32_e32 v61, 2, v61
	s_nop 1
	v_mov_b32_dpp v62, v38 quad_perm:[2,3,0,1] row_mask:0xf bank_mask:0xf
	s_waitcnt lgkmcnt(0)
	v_add_f32_e32 v38, v38, v62
	v_xor_b32_e32 v62, 4, v195
	v_cmp_lt_i32_e32 vcc, v62, v39
	s_nop 1
	v_cndmask_b32_e32 v62, v195, v62, vcc
	v_lshlrev_b32_e32 v62, 2, v62
	s_nop 1
	v_mov_b32_dpp v63, v38 row_half_mirror row_mask:0xf bank_mask:0xf
	s_waitcnt lgkmcnt(0)
	v_add_f32_e32 v38, v38, v63
	v_xor_b32_e32 v63, 8, v195
	v_cmp_lt_i32_e32 vcc, v63, v39
	s_nop 1
	v_cndmask_b32_e32 v63, v195, v63, vcc
	v_lshlrev_b32_e32 v63, 2, v63
	s_nop 1
	v_mov_b32_dpp v138, v38 row_mirror row_mask:0xf bank_mask:0xf
	s_waitcnt lgkmcnt(0)
	v_add_f32_e32 v38, v38, v138
	v_xor_b32_e32 v138, 16, v195
	v_cmp_lt_i32_e32 vcc, v138, v39
	s_nop 1
	v_cndmask_b32_e32 v138, v195, v138, vcc
	v_lshlrev_b32_e32 v161, 2, v138
	ds_bpermute_b32 v138, v161, v38
	s_waitcnt lgkmcnt(0)
	v_add_f32_e32 v38, v38, v138
	v_xor_b32_e32 v138, 32, v195
	v_cmp_lt_i32_e32 vcc, v138, v39
	s_nop 1
	v_cndmask_b32_e32 v39, v195, v138, vcc
	v_lshlrev_b32_e32 v162, 2, v39
	ds_bpermute_b32 v39, v162, v38
	s_waitcnt lgkmcnt(0)
	v_add_f32_e32 v38, v38, v39
	v_mul_f32_e32 v38, 0x3a000000, v38
	v_pk_add_f32 v[230:231], v[164:165], v[38:39] op_sel_hi:[1,0] neg_lo:[0,1] neg_hi:[0,1]
	v_pk_add_f32 v[56:57], v[56:57], v[38:39] op_sel_hi:[1,0] neg_lo:[0,1] neg_hi:[0,1]
	v_pk_mul_f32 v[164:165], v[230:231], v[230:231]
	v_pk_mul_f32 v[170:171], v[56:57], v[56:57]
	v_pk_add_f32 v[250:251], v[46:47], v[38:39] op_sel_hi:[1,0] neg_lo:[0,1] neg_hi:[0,1]
	v_add_f32_e32 v46, v164, v165
	v_pk_add_f32 v[228:229], v[166:167], v[38:39] op_sel_hi:[1,0] neg_lo:[0,1] neg_hi:[0,1]
	v_add_f32_e32 v46, v170, v46
	v_pk_mul_f32 v[166:167], v[228:229], v[228:229]
	v_add_f32_e32 v46, v171, v46
	v_pk_add_f32 v[226:227], v[58:59], v[38:39] op_sel_hi:[1,0] neg_lo:[0,1] neg_hi:[0,1]
	v_add_f32_e32 v46, v166, v46
	v_pk_mul_f32 v[58:59], v[226:227], v[226:227]
	v_add_f32_e32 v46, v167, v46
	v_pk_add_f32 v[236:237], v[168:169], v[38:39] op_sel_hi:[1,0] neg_lo:[0,1] neg_hi:[0,1]
	v_add_f32_e32 v46, v58, v46
	v_pk_mul_f32 v[168:169], v[236:237], v[236:237]
	v_add_f32_e32 v46, v59, v46
	v_pk_add_f32 v[48:49], v[48:49], v[38:39] op_sel_hi:[1,0] neg_lo:[0,1] neg_hi:[0,1]
	v_add_f32_e32 v46, v168, v46
	v_pk_mul_f32 v[172:173], v[48:49], v[48:49]
	v_add_f32_e32 v46, v169, v46
	v_pk_add_f32 v[234:235], v[52:53], v[38:39] op_sel_hi:[1,0] neg_lo:[0,1] neg_hi:[0,1]
	v_add_f32_e32 v46, v172, v46
	v_pk_mul_f32 v[52:53], v[234:235], v[234:235]
	v_add_f32_e32 v46, v173, v46
	v_pk_add_f32 v[232:233], v[50:51], v[38:39] op_sel_hi:[1,0] neg_lo:[0,1] neg_hi:[0,1]
	v_add_f32_e32 v46, v52, v46
	v_pk_mul_f32 v[50:51], v[232:233], v[232:233]
	v_add_f32_e32 v46, v53, v46
	v_pk_add_f32 v[244:245], v[54:55], v[38:39] op_sel_hi:[1,0] neg_lo:[0,1] neg_hi:[0,1]
	v_add_f32_e32 v46, v50, v46
	v_pk_mul_f32 v[54:55], v[244:245], v[244:245]
	v_add_f32_e32 v46, v51, v46
	v_pk_add_f32 v[242:243], v[40:41], v[38:39] op_sel_hi:[1,0] neg_lo:[0,1] neg_hi:[0,1]
	v_add_f32_e32 v46, v54, v46
	v_pk_mul_f32 v[40:41], v[242:243], v[242:243]
	v_add_f32_e32 v46, v55, v46
	v_pk_add_f32 v[240:241], v[44:45], v[38:39] op_sel_hi:[1,0] neg_lo:[0,1] neg_hi:[0,1]
	v_add_f32_e32 v40, v40, v46
	v_pk_mul_f32 v[44:45], v[240:241], v[240:241]
	v_add_f32_e32 v40, v41, v40
	v_pk_add_f32 v[238:239], v[42:43], v[38:39] op_sel_hi:[1,0] neg_lo:[0,1] neg_hi:[0,1]
	v_add_f32_e32 v40, v44, v40
	v_pk_mul_f32 v[42:43], v[238:239], v[238:239]
	v_add_f32_e32 v40, v45, v40
	v_add_f32_e32 v40, v42, v40
	v_pk_add_f32 v[184:185], v[34:35], v[38:39] op_sel_hi:[1,0] neg_lo:[0,1] neg_hi:[0,1]
	v_pk_add_f32 v[246:247], v[36:37], v[38:39] op_sel_hi:[1,0] neg_lo:[0,1] neg_hi:[0,1]
	v_pk_add_f32 v[248:249], v[32:33], v[38:39] op_sel_hi:[1,0] neg_lo:[0,1] neg_hi:[0,1]
	v_pk_mul_f32 v[38:39], v[250:251], v[250:251]
	v_add_f32_e32 v40, v43, v40
	v_add_f32_e32 v38, v38, v40
	v_pk_mul_f32 v[32:33], v[248:249], v[248:249]
	v_add_f32_e32 v38, v39, v38
	v_add_f32_e32 v32, v32, v38
	v_pk_mul_f32 v[36:37], v[246:247], v[246:247]
	v_add_f32_e32 v32, v33, v32
	v_add_f32_e32 v32, v36, v32
	v_pk_mul_f32 v[34:35], v[184:185], v[184:185]
	v_add_f32_e32 v32, v37, v32
	v_add_f32_e32 v32, v34, v32
	v_add_f32_e32 v32, v35, v32
	s_nop 1
	v_mov_b32_dpp v33, v32 quad_perm:[1,0,3,2] row_mask:0xf bank_mask:0xf
	s_waitcnt lgkmcnt(0)
	v_add_f32_e32 v32, v32, v33
	s_nop 1
	v_mov_b32_dpp v33, v32 quad_perm:[2,3,0,1] row_mask:0xf bank_mask:0xf
	s_waitcnt lgkmcnt(0)
	v_add_f32_e32 v32, v32, v33
	s_nop 1
	v_mov_b32_dpp v33, v32 row_half_mirror row_mask:0xf bank_mask:0xf
	s_waitcnt lgkmcnt(0)
	v_add_f32_e32 v50, v32, v33
	s_nop 1
	v_mov_b32_dpp v51, v50 row_mirror row_mask:0xf bank_mask:0xf
	ds_read_b128 v[32:35], v75
	ds_read_b128 v[36:39], v76
	ds_read_b128 v[40:43], v77
	ds_read_b128 v[44:47], v78
	s_waitcnt lgkmcnt(4)
	v_add_f32_e32 v54, v50, v51
	ds_bpermute_b32 v55, v161, v54
	ds_read_b128 v[50:53], v79
	ds_read_b128 v[164:167], v80
	ds_read_b128 v[168:171], v81
	ds_read_b128 v[172:175], v82
	ds_read_b128 v[176:179], v83
	ds_read_b128 v[180:183], v84
	ds_read_b128 v[202:205], v85
	ds_read_b128 v[206:209], v86
	ds_read_b128 v[210:213], v87
	ds_read_b128 v[214:217], v88
	ds_read_b128 v[218:221], v89
	ds_read_b128 v[222:225], v90
	s_waitcnt lgkmcnt(12)
	v_add_f32_e32 v54, v54, v55
	ds_bpermute_b32 v55, v162, v54
	s_waitcnt lgkmcnt(0)
	v_add_f32_e32 v54, v54, v55
	v_fmamk_f32 v54, v54, 0x3a000000, v192
	v_mul_f32_e32 v55, 0x4f800000, v54
	v_cmp_gt_f32_e32 vcc, s88, v54
	s_nop 1
	v_cndmask_b32_e32 v54, v54, v55, vcc
	v_sqrt_f32_e32 v55, v54
	s_nop 0
	v_add_u32_e32 v58, -1, v55
	v_fma_f32 v59, -v58, v55, v54
	v_cmp_ge_f32_e64 s[42:43], 0, v59
	v_add_u32_e32 v59, 1, v55
	s_nop 0
	v_cndmask_b32_e64 v58, v55, v58, s[42:43]
	v_fma_f32 v55, -v59, v55, v54
	v_cmp_lt_f32_e64 s[42:43], 0, v55
	s_nop 1
	v_cndmask_b32_e64 v55, v58, v59, s[42:43]
	v_mul_f32_e32 v58, 0x37800000, v55
	v_cndmask_b32_e32 v55, v55, v58, vcc
	v_cmp_class_f32_e32 vcc, v54, v191
	s_nop 1
	v_cndmask_b32_e32 v54, v55, v54, vcc
	v_div_scale_f32 v55, s[12:13], v54, v54, 1.0
	v_rcp_f32_e32 v58, v55
	s_lshl_b64 s[12:13], s[6:7], 12
	v_lshl_add_u64 v[188:189], v[64:65], 0, s[12:13]
	s_add_i32 s7, 0, 0x25000
	v_fma_f32 v59, -v55, v58, 1.0
	v_fmac_f32_e32 v58, v59, v58
	v_div_scale_f32 v59, vcc, 1.0, v54, 1.0
	v_mul_f32_e32 v138, v59, v58
	v_fma_f32 v139, -v55, v138, v59
	v_fmac_f32_e32 v138, v139, v58
	v_fma_f32 v55, -v55, v138, v59
	v_div_fmas_f32 v55, v55, v58, v138
	v_div_fixup_f32 v138, v55, v54, 1.0
	v_pk_mul_f32 v[54:55], v[230:231], v[138:139] op_sel_hi:[1,0]
	s_nop 0
	v_pk_fma_f32 v[230:231], v[32:33], v[54:55], v[40:41]
	v_pk_mul_f32 v[32:33], v[228:229], v[138:139] op_sel_hi:[1,0]
	s_nop 0
	v_pk_fma_f32 v[58:59], v[36:37], v[32:33], v[44:45]
	v_pk_mul_f32 v[32:33], v[56:57], v[138:139] op_sel_hi:[1,0]
	s_nop 0
	v_pk_fma_f32 v[228:229], v[34:35], v[32:33], v[42:43]
	v_pk_mul_f32 v[32:33], v[226:227], v[138:139] op_sel_hi:[1,0]
	s_nop 0
	v_pk_fma_f32 v[56:57], v[38:39], v[32:33], v[46:47]
	v_pk_mul_f32 v[32:33], v[236:237], v[138:139] op_sel_hi:[1,0]
	s_nop 0
	v_pk_fma_f32 v[54:55], v[50:51], v[32:33], v[168:169]
	v_pk_mul_f32 v[32:33], v[234:235], v[138:139] op_sel_hi:[1,0]
	s_nop 0
	v_pk_fma_f32 v[50:51], v[164:165], v[32:33], v[172:173]
	v_pk_mul_f32 v[32:33], v[48:49], v[138:139] op_sel_hi:[1,0]
	v_cvt_pk_bf16_f32 v164, v230, v231
	v_pk_fma_f32 v[52:53], v[52:53], v[32:33], v[170:171]
	v_pk_mul_f32 v[32:33], v[232:233], v[138:139] op_sel_hi:[1,0]
	v_cvt_pk_bf16_f32 v165, v228, v229
	v_pk_fma_f32 v[48:49], v[166:167], v[32:33], v[174:175]
	v_pk_mul_f32 v[32:33], v[244:245], v[138:139] op_sel_hi:[1,0]
	v_cvt_pk_bf16_f32 v166, v58, v59
	v_pk_fma_f32 v[46:47], v[176:177], v[32:33], v[202:203]
	v_pk_mul_f32 v[32:33], v[240:241], v[138:139] op_sel_hi:[1,0]
	v_cvt_pk_bf16_f32 v167, v56, v57
	v_pk_fma_f32 v[42:43], v[180:181], v[32:33], v[206:207]
	v_pk_mul_f32 v[32:33], v[242:243], v[138:139] op_sel_hi:[1,0]
	global_store_dwordx4 v[188:189], v[164:167], off
	v_pk_fma_f32 v[44:45], v[178:179], v[32:33], v[204:205]
	v_pk_mul_f32 v[32:33], v[238:239], v[138:139] op_sel_hi:[1,0]
	v_cvt_pk_bf16_f32 v164, v54, v55
	v_pk_fma_f32 v[40:41], v[182:183], v[32:33], v[208:209]
	v_pk_mul_f32 v[32:33], v[250:251], v[138:139] op_sel_hi:[1,0]
	v_cvt_pk_bf16_f32 v165, v52, v53
	v_pk_fma_f32 v[38:39], v[210:211], v[32:33], v[218:219]
	v_pk_mul_f32 v[32:33], v[246:247], v[138:139] op_sel_hi:[1,0]
	v_cvt_pk_bf16_f32 v166, v50, v51
	v_pk_fma_f32 v[34:35], v[214:215], v[32:33], v[222:223]
	v_pk_mul_f32 v[32:33], v[248:249], v[138:139] op_sel_hi:[1,0]
	v_cvt_pk_bf16_f32 v167, v48, v49
	v_pk_fma_f32 v[36:37], v[212:213], v[32:33], v[220:221]
	v_pk_mul_f32 v[32:33], v[184:185], v[138:139] op_sel_hi:[1,0]
	global_store_dwordx4 v[188:189], v[164:167], off offset:1024
	v_pk_fma_f32 v[32:33], v[216:217], v[32:33], v[224:225]
	s_nop 0
	v_cvt_pk_bf16_f32 v164, v46, v47
	v_cvt_pk_bf16_f32 v165, v44, v45
	v_cvt_pk_bf16_f32 v166, v42, v43
	v_cvt_pk_bf16_f32 v167, v40, v41
	global_store_dwordx4 v[188:189], v[164:167], off offset:2048
	s_nop 1
	v_cvt_pk_bf16_f32 v164, v38, v39
	v_cvt_pk_bf16_f32 v165, v36, v37
	v_cvt_pk_bf16_f32 v166, v34, v35
	v_cvt_pk_bf16_f32 v167, v32, v33
	global_store_dwordx4 v[188:189], v[164:167], off offset:3072
	ds_read_b128 v[164:167], v72
	ds_read_b128 v[168:171], v72 offset:1024
	ds_read_b128 v[180:183], v72 offset:3072
	s_waitcnt lgkmcnt(2)
	v_fma_f32 v177, v164, v230, 0
	v_fma_f32 v178, v165, v230, 0
	v_fma_f32 v176, v166, v230, 0
	v_fma_f32 v175, v167, v230, 0
	ds_read_b128 v[164:167], v72 offset:2048
	s_waitcnt lgkmcnt(2)
	v_fma_f32 v174, v168, v230, 0
	v_fma_f32 v173, v169, v230, 0
	v_fma_f32 v172, v170, v230, 0
	s_waitcnt lgkmcnt(1)
	v_fma_f32 v163, v181, v230, 0
	s_waitcnt lgkmcnt(0)
	v_fma_f32 v170, v164, v230, 0
	v_fma_f32 v169, v165, v230, 0
	v_fma_f32 v168, v166, v230, 0
	v_fma_f32 v166, v180, v230, 0
	ds_read_b128 v[202:205], v72 offset:5120
	ds_read_b128 v[206:209], v72 offset:4096
	v_fma_f32 v165, v182, v230, 0
	v_fma_f32 v164, v183, v230, 0
	ds_read_b128 v[180:183], v72 offset:7168
	ds_read_b128 v[210:213], v72 offset:6144
	v_fma_f32 v171, v171, v230, 0
	s_waitcnt lgkmcnt(3)
	v_fmac_f32_e32 v174, v202, v231
	v_fmac_f32_e32 v173, v203, v231
	v_fmac_f32_e32 v172, v204, v231
	v_fmac_f32_e32 v171, v205, v231
	s_waitcnt lgkmcnt(1)
	v_fmac_f32_e32 v166, v180, v231
	ds_read_b128 v[202:205], v72 offset:8192
	v_fmac_f32_e32 v163, v181, v231
	v_fmac_f32_e32 v165, v182, v231
	v_fmac_f32_e32 v164, v183, v231
	ds_read_b128 v[180:183], v72 offset:9216
	v_fmac_f32_e32 v177, v206, v231
	v_fmac_f32_e32 v178, v207, v231
	v_fmac_f32_e32 v176, v208, v231
	v_fmac_f32_e32 v175, v209, v231
	s_waitcnt lgkmcnt(1)
	v_fmac_f32_e32 v177, v202, v228
	v_fmac_f32_e32 v178, v203, v228
	v_fmac_f32_e32 v176, v204, v228
	v_fmac_f32_e32 v175, v205, v228
	s_waitcnt lgkmcnt(0)
	v_fmac_f32_e32 v174, v180, v228
	ds_read_b128 v[202:205], v72 offset:10240
	v_fmac_f32_e32 v173, v181, v228
	v_fmac_f32_e32 v172, v182, v228
	v_fmac_f32_e32 v171, v183, v228
	ds_read_b128 v[180:183], v72 offset:11264
	v_fma_f32 v167, v167, v230, 0
	v_fmac_f32_e32 v170, v210, v231
	v_fmac_f32_e32 v169, v211, v231
	v_fmac_f32_e32 v168, v212, v231
	v_fmac_f32_e32 v167, v213, v231
	s_waitcnt lgkmcnt(1)
	v_fmac_f32_e32 v170, v202, v228
	v_fmac_f32_e32 v169, v203, v228
	v_fmac_f32_e32 v168, v204, v228
	v_fmac_f32_e32 v167, v205, v228
	s_waitcnt lgkmcnt(0)
	v_fmac_f32_e32 v166, v180, v228
	v_fmac_f32_e32 v163, v181, v228
	ds_read_b128 v[202:205], v72 offset:13312
	ds_read_b128 v[206:209], v72 offset:12288
	v_fmac_f32_e32 v165, v182, v228
	v_fmac_f32_e32 v164, v183, v228
	ds_read_b128 v[180:183], v72 offset:15360
	ds_read_b128 v[210:213], v72 offset:14336
	s_waitcnt lgkmcnt(3)
	v_fmac_f32_e32 v174, v202, v229
	v_fmac_f32_e32 v173, v203, v229
	v_fmac_f32_e32 v172, v204, v229
	v_fmac_f32_e32 v171, v205, v229
	s_waitcnt lgkmcnt(1)
	v_fmac_f32_e32 v166, v180, v229
	ds_read_b128 v[202:205], v72 offset:16384
	v_fmac_f32_e32 v163, v181, v229
	v_fmac_f32_e32 v165, v182, v229
	v_fmac_f32_e32 v164, v183, v229
	ds_read_b128 v[180:183], v72 offset:17408
	v_fmac_f32_e32 v177, v206, v229
	v_fmac_f32_e32 v178, v207, v229
	v_fmac_f32_e32 v176, v208, v229
	v_fmac_f32_e32 v175, v209, v229
	s_waitcnt lgkmcnt(1)
	v_fmac_f32_e32 v177, v202, v58
	v_fmac_f32_e32 v178, v203, v58
	v_fmac_f32_e32 v176, v204, v58
	v_fmac_f32_e32 v175, v205, v58
	s_waitcnt lgkmcnt(0)
	v_fmac_f32_e32 v174, v180, v58
	ds_read_b128 v[202:205], v72 offset:18432
	v_fmac_f32_e32 v173, v181, v58
	v_fmac_f32_e32 v172, v182, v58
	v_fmac_f32_e32 v171, v183, v58
	ds_read_b128 v[180:183], v72 offset:19456
	v_fmac_f32_e32 v170, v210, v229
	v_fmac_f32_e32 v169, v211, v229
	v_fmac_f32_e32 v168, v212, v229
	v_fmac_f32_e32 v167, v213, v229
	s_waitcnt lgkmcnt(1)
	v_fmac_f32_e32 v170, v58, v202
	v_fmac_f32_e32 v169, v58, v203
	v_fmac_f32_e32 v168, v58, v204
	v_fmac_f32_e32 v167, v58, v205
	s_waitcnt lgkmcnt(0)
	v_fmac_f32_e32 v166, v58, v180
	v_fmac_f32_e32 v163, v58, v181
	ds_read_b128 v[202:205], v72 offset:21504
	ds_read_b128 v[206:209], v72 offset:20480
	v_fmac_f32_e32 v165, v58, v182
	v_fmac_f32_e32 v164, v58, v183
	ds_read_b128 v[180:183], v72 offset:23552
	ds_read_b128 v[210:213], v72 offset:22528
	s_waitcnt lgkmcnt(3)
	v_fmac_f32_e32 v174, v59, v202
	v_fmac_f32_e32 v173, v59, v203
	v_fmac_f32_e32 v172, v59, v204
	v_fmac_f32_e32 v171, v59, v205
	s_waitcnt lgkmcnt(1)
	v_fmac_f32_e32 v166, v59, v180
	ds_read_b128 v[202:205], v72 offset:24576
	v_fmac_f32_e32 v163, v59, v181
	v_fmac_f32_e32 v165, v59, v182
	v_fmac_f32_e32 v164, v59, v183
	ds_read_b128 v[180:183], v72 offset:25600
	v_fmac_f32_e32 v177, v59, v206
	v_fmac_f32_e32 v178, v59, v207
	v_fmac_f32_e32 v176, v59, v208
	v_fmac_f32_e32 v175, v59, v209
	s_waitcnt lgkmcnt(1)
	v_fmac_f32_e32 v177, v56, v202
	v_fmac_f32_e32 v178, v56, v203
	v_fmac_f32_e32 v176, v56, v204
	v_fmac_f32_e32 v175, v56, v205
	s_waitcnt lgkmcnt(0)
	v_fmac_f32_e32 v174, v56, v180
	ds_read_b128 v[202:205], v72 offset:26624
	v_fmac_f32_e32 v173, v56, v181
	v_fmac_f32_e32 v172, v56, v182
	v_fmac_f32_e32 v171, v56, v183
	ds_read_b128 v[180:183], v72 offset:27648
	v_fmac_f32_e32 v170, v59, v210
	v_fmac_f32_e32 v169, v59, v211
	v_fmac_f32_e32 v168, v59, v212
	v_fmac_f32_e32 v167, v59, v213
	s_waitcnt lgkmcnt(1)
	v_fmac_f32_e32 v170, v56, v202
	v_fmac_f32_e32 v169, v56, v203
	v_fmac_f32_e32 v168, v56, v204
	v_fmac_f32_e32 v167, v56, v205
	s_waitcnt lgkmcnt(0)
	v_fmac_f32_e32 v166, v56, v180
	v_fmac_f32_e32 v163, v56, v181
	ds_read_b128 v[202:205], v72 offset:29696
	ds_read_b128 v[206:209], v72 offset:28672
	v_fmac_f32_e32 v165, v56, v182
	v_fmac_f32_e32 v164, v56, v183
	ds_read_b128 v[180:183], v72 offset:31744
	ds_read_b128 v[210:213], v72 offset:30720
	s_waitcnt lgkmcnt(2)
	v_fmac_f32_e32 v177, v57, v206
	v_fmac_f32_e32 v178, v57, v207
	v_fmac_f32_e32 v176, v57, v208
	v_fmac_f32_e32 v175, v57, v209
	v_fmac_f32_e32 v174, v57, v202
	v_fmac_f32_e32 v173, v57, v203
	v_fmac_f32_e32 v172, v57, v204
	v_fmac_f32_e32 v171, v57, v205
	s_waitcnt lgkmcnt(0)
	v_fmac_f32_e32 v170, v57, v210
	v_fmac_f32_e32 v169, v57, v211
	v_fmac_f32_e32 v168, v57, v212
	v_fmac_f32_e32 v167, v57, v213
	v_fmac_f32_e32 v166, v57, v180
	ds_read_b128 v[202:205], v72 offset:32768
	v_fmac_f32_e32 v163, v57, v181
	v_fmac_f32_e32 v165, v57, v182
	v_fmac_f32_e32 v164, v57, v183
	ds_read_b128 v[56:59], v72 offset:33792
	ds_read_b128 v[180:183], v72 offset:34816
	s_waitcnt lgkmcnt(2)
	v_fmac_f32_e32 v177, v54, v202
	v_fmac_f32_e32 v178, v54, v203
	v_fmac_f32_e32 v176, v54, v204
	s_waitcnt lgkmcnt(1)
	v_fmac_f32_e32 v174, v54, v56
	v_fmac_f32_e32 v173, v54, v57
	v_fmac_f32_e32 v172, v54, v58
	v_fmac_f32_e32 v171, v54, v59
	ds_read_b128 v[56:59], v72 offset:35840
	v_fmac_f32_e32 v175, v54, v205
	s_waitcnt lgkmcnt(1)
	v_fmac_f32_e32 v170, v54, v180
	v_fmac_f32_e32 v169, v54, v181
	v_fmac_f32_e32 v168, v54, v182
	v_fmac_f32_e32 v167, v54, v183
	s_waitcnt lgkmcnt(0)
	v_fmac_f32_e32 v166, v54, v56
	v_fmac_f32_e32 v163, v54, v57
	ds_read_b128 v[180:183], v72 offset:37888
	ds_read_b128 v[202:205], v72 offset:36864
	v_fmac_f32_e32 v165, v54, v58
	v_fmac_f32_e32 v164, v54, v59
	ds_read_b128 v[56:59], v72 offset:39936
	ds_read_b128 v[206:209], v72 offset:38912
	s_waitcnt lgkmcnt(2)
	v_fmac_f32_e32 v177, v55, v202
	v_fmac_f32_e32 v178, v55, v203
	v_fmac_f32_e32 v176, v55, v204
	v_fmac_f32_e32 v175, v55, v205
	v_fmac_f32_e32 v174, v55, v180
	v_fmac_f32_e32 v173, v55, v181
	v_fmac_f32_e32 v172, v55, v182
	v_fmac_f32_e32 v171, v55, v183
	s_waitcnt lgkmcnt(0)
	v_fmac_f32_e32 v170, v55, v206
	v_fmac_f32_e32 v169, v55, v207
	v_fmac_f32_e32 v168, v55, v208
	v_fmac_f32_e32 v167, v55, v209
	v_fmac_f32_e32 v166, v55, v56
	ds_read_b128 v[180:183], v72 offset:40960
	v_fmac_f32_e32 v163, v55, v57
	v_fmac_f32_e32 v165, v55, v58
	v_fmac_f32_e32 v164, v55, v59
	ds_read_b128 v[54:57], v72 offset:41984
	s_waitcnt lgkmcnt(1)
	v_fmac_f32_e32 v177, v52, v180
	v_fmac_f32_e32 v178, v52, v181
	v_fmac_f32_e32 v176, v52, v182
	v_fmac_f32_e32 v175, v52, v183
	s_waitcnt lgkmcnt(0)
	v_fmac_f32_e32 v174, v52, v54
	ds_read_b128 v[180:183], v72 offset:43008
	v_fmac_f32_e32 v173, v52, v55
	v_fmac_f32_e32 v172, v52, v56
	v_fmac_f32_e32 v171, v52, v57
	ds_read_b128 v[54:57], v72 offset:44032
	s_waitcnt lgkmcnt(1)
	v_fmac_f32_e32 v170, v52, v180
	v_fmac_f32_e32 v169, v52, v181
	v_fmac_f32_e32 v168, v52, v182
	v_fmac_f32_e32 v167, v52, v183
	s_waitcnt lgkmcnt(0)
	v_fmac_f32_e32 v166, v52, v54
	v_fmac_f32_e32 v163, v52, v55
	ds_read_b128 v[180:183], v72 offset:46080
	ds_read_b128 v[202:205], v72 offset:45056
	v_fmac_f32_e32 v165, v52, v56
	v_fmac_f32_e32 v164, v52, v57
	ds_read_b128 v[54:57], v72 offset:48128
	ds_read_b128 v[206:209], v72 offset:47104
	s_waitcnt lgkmcnt(2)
	v_fmac_f32_e32 v177, v53, v202
	v_fmac_f32_e32 v178, v53, v203
	v_fmac_f32_e32 v176, v53, v204
	v_fmac_f32_e32 v175, v53, v205
	v_fmac_f32_e32 v174, v53, v180
	v_fmac_f32_e32 v173, v53, v181
	v_fmac_f32_e32 v172, v53, v182
	v_fmac_f32_e32 v171, v53, v183
	s_waitcnt lgkmcnt(0)
	v_fmac_f32_e32 v170, v53, v206
	v_fmac_f32_e32 v169, v53, v207
	v_fmac_f32_e32 v168, v53, v208
	v_fmac_f32_e32 v167, v53, v209
	v_fmac_f32_e32 v166, v53, v54
	ds_read_b128 v[180:183], v72 offset:49152
	v_fmac_f32_e32 v163, v53, v55
	v_fmac_f32_e32 v165, v53, v56
	v_fmac_f32_e32 v164, v53, v57
	ds_read_b128 v[52:55], v72 offset:50176
	ds_read_b128 v[56:59], v72 offset:51200
	s_waitcnt lgkmcnt(2)
	v_fmac_f32_e32 v177, v50, v180
	v_fmac_f32_e32 v178, v50, v181
	v_fmac_f32_e32 v176, v50, v182
	s_waitcnt lgkmcnt(1)
	v_fmac_f32_e32 v174, v50, v52
	v_fmac_f32_e32 v173, v50, v53
	v_fmac_f32_e32 v172, v50, v54
	v_fmac_f32_e32 v171, v50, v55
	ds_read_b128 v[52:55], v72 offset:52224
	v_fmac_f32_e32 v175, v50, v183
	s_waitcnt lgkmcnt(1)
	v_fmac_f32_e32 v170, v50, v56
	v_fmac_f32_e32 v169, v50, v57
	v_fmac_f32_e32 v168, v50, v58
	v_fmac_f32_e32 v167, v50, v59
	s_waitcnt lgkmcnt(0)
	v_fmac_f32_e32 v166, v50, v52
	v_fmac_f32_e32 v163, v50, v53
	ds_read_b128 v[56:59], v72 offset:54272
	ds_read_b128 v[180:183], v72 offset:53248
	v_fmac_f32_e32 v165, v50, v54
	v_fmac_f32_e32 v164, v50, v55
	ds_read_b128 v[52:55], v72 offset:56320
	ds_read_b128 v[202:205], v72 offset:55296
	s_waitcnt lgkmcnt(2)
	v_fmac_f32_e32 v177, v51, v180
	v_fmac_f32_e32 v178, v51, v181
	v_fmac_f32_e32 v176, v51, v182
	v_fmac_f32_e32 v175, v51, v183
	v_fmac_f32_e32 v174, v51, v56
	v_fmac_f32_e32 v173, v51, v57
	v_fmac_f32_e32 v172, v51, v58
	v_fmac_f32_e32 v171, v51, v59
	s_waitcnt lgkmcnt(0)
	v_fmac_f32_e32 v170, v51, v202
	v_fmac_f32_e32 v169, v51, v203
	v_fmac_f32_e32 v168, v51, v204
	v_fmac_f32_e32 v167, v51, v205
	v_fmac_f32_e32 v166, v51, v52
	ds_read_b128 v[56:59], v72 offset:57344
	v_fmac_f32_e32 v163, v51, v53
	v_fmac_f32_e32 v165, v51, v54
	v_fmac_f32_e32 v164, v51, v55
	ds_read_b128 v[50:53], v72 offset:58368
	s_waitcnt lgkmcnt(1)
	v_fmac_f32_e32 v177, v48, v56
	v_fmac_f32_e32 v178, v48, v57
	ds_read_b128 v[54:57], v72 offset:59392
	v_fmac_f32_e32 v176, v48, v58
	s_waitcnt lgkmcnt(1)
	v_fmac_f32_e32 v174, v48, v50
	v_fmac_f32_e32 v173, v48, v51
	v_fmac_f32_e32 v172, v48, v52
	v_fmac_f32_e32 v171, v48, v53
	ds_read_b128 v[50:53], v72 offset:60416
	s_waitcnt lgkmcnt(1)
	v_fmac_f32_e32 v170, v48, v54
	v_fmac_f32_e32 v169, v48, v55
	v_fmac_f32_e32 v168, v48, v56
	v_fmac_f32_e32 v167, v48, v57
	s_waitcnt lgkmcnt(0)
	v_fmac_f32_e32 v166, v48, v50
	v_fmac_f32_e32 v163, v48, v51
	ds_read_b128 v[54:57], v72 offset:62464
	ds_read_b128 v[180:183], v72 offset:61440
	v_fmac_f32_e32 v165, v48, v52
	v_fmac_f32_e32 v164, v48, v53
	ds_read_b128 v[50:53], v72 offset:64512
	ds_read_b128 v[202:205], v72 offset:63488
	v_fmac_f32_e32 v175, v48, v59
	s_waitcnt lgkmcnt(2)
	v_fmac_f32_e32 v177, v49, v180
	v_fmac_f32_e32 v178, v49, v181
	v_fmac_f32_e32 v176, v49, v182
	v_fmac_f32_e32 v175, v49, v183
	v_fmac_f32_e32 v174, v49, v54
	v_fmac_f32_e32 v173, v49, v55
	v_fmac_f32_e32 v172, v49, v56
	v_fmac_f32_e32 v171, v49, v57
	s_waitcnt lgkmcnt(0)
	v_fmac_f32_e32 v170, v49, v202
	v_fmac_f32_e32 v169, v49, v203
	v_fmac_f32_e32 v168, v49, v204
	v_fmac_f32_e32 v167, v49, v205
	v_fmac_f32_e32 v166, v49, v50
	ds_read_b128 v[54:57], v91
	v_fmac_f32_e32 v163, v49, v51
	v_fmac_f32_e32 v165, v49, v52
	v_fmac_f32_e32 v164, v49, v53
	ds_read_b128 v[48:51], v92
	s_waitcnt lgkmcnt(1)
	v_fmac_f32_e32 v177, v46, v54
	v_fmac_f32_e32 v178, v46, v55
	ds_read_b128 v[52:55], v93
	v_fmac_f32_e32 v176, v46, v56
	s_waitcnt lgkmcnt(1)
	v_fmac_f32_e32 v174, v46, v48
	v_fmac_f32_e32 v173, v46, v49
	v_fmac_f32_e32 v172, v46, v50
	v_fmac_f32_e32 v171, v46, v51
	ds_read_b128 v[48:51], v94
	v_fmac_f32_e32 v175, v46, v57
	s_waitcnt lgkmcnt(1)
	v_fmac_f32_e32 v170, v46, v52
	v_fmac_f32_e32 v169, v46, v53
	v_fmac_f32_e32 v168, v46, v54
	v_fmac_f32_e32 v167, v46, v55
	s_waitcnt lgkmcnt(0)
	v_fmac_f32_e32 v166, v46, v48
	v_fmac_f32_e32 v163, v46, v49
	ds_read_b128 v[52:55], v95
	ds_read_b128 v[56:59], v96
	v_fmac_f32_e32 v165, v46, v50
	v_fmac_f32_e32 v164, v46, v51
	ds_read_b128 v[48:51], v97
	ds_read_b128 v[180:183], v98
	s_waitcnt lgkmcnt(3)
	v_fmac_f32_e32 v166, v47, v52
	v_fmac_f32_e32 v163, v47, v53
	s_waitcnt lgkmcnt(1)
	v_fmac_f32_e32 v170, v47, v48
	v_fmac_f32_e32 v169, v47, v49
	v_fmac_f32_e32 v168, v47, v50
	v_fmac_f32_e32 v167, v47, v51
	ds_read_b128 v[48:51], v99
	v_fmac_f32_e32 v165, v47, v54
	v_fmac_f32_e32 v164, v47, v55
	ds_read_b128 v[52:55], v100
	v_fmac_f32_e32 v177, v47, v56
	v_fmac_f32_e32 v178, v47, v57
	v_fmac_f32_e32 v176, v47, v58
	v_fmac_f32_e32 v175, v47, v59
	s_waitcnt lgkmcnt(2)
	v_fmac_f32_e32 v174, v47, v180
	v_fmac_f32_e32 v173, v47, v181
	v_fmac_f32_e32 v172, v47, v182
	v_fmac_f32_e32 v171, v47, v183
	s_waitcnt lgkmcnt(1)
	v_fmac_f32_e32 v177, v44, v48
	v_fmac_f32_e32 v178, v44, v49
	v_fmac_f32_e32 v176, v44, v50
	v_fmac_f32_e32 v175, v44, v51
	s_waitcnt lgkmcnt(0)
	v_fmac_f32_e32 v174, v44, v52
	ds_read_b128 v[46:49], v101
	v_fmac_f32_e32 v173, v44, v53
	ds_read_b128 v[50:53], v102
	v_fmac_f32_e32 v172, v44, v54
	v_fmac_f32_e32 v171, v44, v55
	s_waitcnt lgkmcnt(1)
	v_fmac_f32_e32 v170, v44, v46
	v_fmac_f32_e32 v169, v44, v47
	v_fmac_f32_e32 v168, v44, v48
	v_fmac_f32_e32 v167, v44, v49
	s_waitcnt lgkmcnt(0)
	v_fmac_f32_e32 v166, v44, v50
	v_fmac_f32_e32 v163, v44, v51
	ds_read_b128 v[46:49], v103
	ds_read_b128 v[54:57], v104
	v_fmac_f32_e32 v165, v44, v52
	v_fmac_f32_e32 v164, v44, v53
	ds_read_b128 v[50:53], v105
	ds_read_b128 v[180:183], v106
	s_waitcnt lgkmcnt(2)
	v_fmac_f32_e32 v177, v45, v54
	v_fmac_f32_e32 v178, v45, v55
	v_fmac_f32_e32 v176, v45, v56
	v_fmac_f32_e32 v175, v45, v57
	s_waitcnt lgkmcnt(0)
	v_fmac_f32_e32 v174, v45, v180
	v_fmac_f32_e32 v173, v45, v181
	v_fmac_f32_e32 v172, v45, v182
	v_fmac_f32_e32 v171, v45, v183
	v_fmac_f32_e32 v170, v45, v50
	v_fmac_f32_e32 v169, v45, v51
	v_fmac_f32_e32 v168, v45, v52
	v_fmac_f32_e32 v167, v45, v53
	v_fmac_f32_e32 v166, v45, v46
	ds_read_b128 v[50:53], v107
	v_fmac_f32_e32 v163, v45, v47
	v_fmac_f32_e32 v165, v45, v48
	v_fmac_f32_e32 v164, v45, v49
	ds_read_b128 v[44:47], v108
	s_waitcnt lgkmcnt(1)
	v_fmac_f32_e32 v177, v42, v50
	v_fmac_f32_e32 v178, v42, v51
	ds_read_b128 v[48:51], v109
	v_fmac_f32_e32 v176, v42, v52
	s_waitcnt lgkmcnt(1)
	v_fmac_f32_e32 v174, v42, v44
	v_fmac_f32_e32 v173, v42, v45
	v_fmac_f32_e32 v172, v42, v46
	v_fmac_f32_e32 v171, v42, v47
	ds_read_b128 v[44:47], v110
	v_fmac_f32_e32 v175, v42, v53
	s_waitcnt lgkmcnt(1)
	v_fmac_f32_e32 v170, v42, v48
	v_fmac_f32_e32 v169, v42, v49
	v_fmac_f32_e32 v168, v42, v50
	v_fmac_f32_e32 v167, v42, v51
	s_waitcnt lgkmcnt(0)
	v_fmac_f32_e32 v166, v42, v44
	v_fmac_f32_e32 v163, v42, v45
	ds_read_b128 v[48:51], v111
	ds_read_b128 v[52:55], v112
	v_fmac_f32_e32 v165, v42, v46
	v_fmac_f32_e32 v164, v42, v47
	ds_read_b128 v[44:47], v113
	ds_read_b128 v[56:59], v114
	s_waitcnt lgkmcnt(3)
	v_fmac_f32_e32 v166, v43, v48
	v_fmac_f32_e32 v163, v43, v49
	s_waitcnt lgkmcnt(1)
	v_fmac_f32_e32 v170, v43, v44
	v_fmac_f32_e32 v169, v43, v45
	v_fmac_f32_e32 v168, v43, v46
	v_fmac_f32_e32 v167, v43, v47
	ds_read_b128 v[44:47], v115
	v_fmac_f32_e32 v165, v43, v50
	v_fmac_f32_e32 v164, v43, v51
	ds_read_b128 v[48:51], v116
	v_fmac_f32_e32 v177, v43, v52
	v_fmac_f32_e32 v178, v43, v53
	v_fmac_f32_e32 v176, v43, v54
	v_fmac_f32_e32 v175, v43, v55
	s_waitcnt lgkmcnt(2)
	v_fmac_f32_e32 v174, v43, v56
	v_fmac_f32_e32 v173, v43, v57
	v_fmac_f32_e32 v172, v43, v58
	v_fmac_f32_e32 v171, v43, v59
	s_waitcnt lgkmcnt(1)
	v_fmac_f32_e32 v177, v40, v44
	v_fmac_f32_e32 v178, v40, v45
	v_fmac_f32_e32 v176, v40, v46
	v_fmac_f32_e32 v175, v40, v47
	s_waitcnt lgkmcnt(0)
	v_fmac_f32_e32 v174, v40, v48
	ds_read_b128 v[42:45], v117
	v_fmac_f32_e32 v173, v40, v49
	ds_read_b128 v[46:49], v118
	v_fmac_f32_e32 v172, v40, v50
	v_fmac_f32_e32 v171, v40, v51
	s_waitcnt lgkmcnt(1)
	v_fmac_f32_e32 v170, v40, v42
	v_fmac_f32_e32 v169, v40, v43
	v_fmac_f32_e32 v168, v40, v44
	v_fmac_f32_e32 v167, v40, v45
	s_waitcnt lgkmcnt(0)
	v_fmac_f32_e32 v166, v40, v46
	v_fmac_f32_e32 v163, v40, v47
	ds_read_b128 v[42:45], v119
	ds_read_b128 v[50:53], v120
	v_fmac_f32_e32 v165, v40, v48
	v_fmac_f32_e32 v164, v40, v49
	ds_read_b128 v[46:49], v121
	ds_read_b128 v[54:57], v122
	s_waitcnt lgkmcnt(2)
	v_fmac_f32_e32 v177, v41, v50
	v_fmac_f32_e32 v178, v41, v51
	v_fmac_f32_e32 v176, v41, v52
	v_fmac_f32_e32 v175, v41, v53
	s_waitcnt lgkmcnt(0)
	v_fmac_f32_e32 v174, v41, v54
	v_fmac_f32_e32 v173, v41, v55
	v_fmac_f32_e32 v172, v41, v56
	v_fmac_f32_e32 v171, v41, v57
	v_fmac_f32_e32 v170, v41, v46
	v_fmac_f32_e32 v169, v41, v47
	v_fmac_f32_e32 v168, v41, v48
	v_fmac_f32_e32 v167, v41, v49
	v_fmac_f32_e32 v166, v41, v42
	ds_read_b128 v[46:49], v123
	v_fmac_f32_e32 v163, v41, v43
	v_fmac_f32_e32 v165, v41, v44
	v_fmac_f32_e32 v164, v41, v45
	ds_read_b128 v[40:43], v124
	s_waitcnt lgkmcnt(1)
	v_fmac_f32_e32 v177, v38, v46
	v_fmac_f32_e32 v178, v38, v47
	ds_read_b128 v[44:47], v125
	v_fmac_f32_e32 v176, v38, v48
	s_waitcnt lgkmcnt(1)
	v_fmac_f32_e32 v174, v38, v40
	v_fmac_f32_e32 v173, v38, v41
	v_fmac_f32_e32 v172, v38, v42
	v_fmac_f32_e32 v171, v38, v43
	ds_read_b128 v[40:43], v126
	v_fmac_f32_e32 v175, v38, v49
	s_waitcnt lgkmcnt(1)
	v_fmac_f32_e32 v170, v38, v44
	v_fmac_f32_e32 v169, v38, v45
	v_fmac_f32_e32 v168, v38, v46
	v_fmac_f32_e32 v167, v38, v47
	s_waitcnt lgkmcnt(0)
	v_fmac_f32_e32 v166, v38, v40
	v_fmac_f32_e32 v163, v38, v41
	ds_read_b128 v[44:47], v127
	ds_read_b128 v[48:51], v128
	v_fmac_f32_e32 v165, v38, v42
	v_fmac_f32_e32 v164, v38, v43
	ds_read_b128 v[40:43], v129
	ds_read_b128 v[52:55], v130
	s_waitcnt lgkmcnt(3)
	v_fmac_f32_e32 v166, v39, v44
	v_fmac_f32_e32 v163, v39, v45
	s_waitcnt lgkmcnt(1)
	v_fmac_f32_e32 v170, v39, v40
	v_fmac_f32_e32 v169, v39, v41
	v_fmac_f32_e32 v168, v39, v42
	v_fmac_f32_e32 v167, v39, v43
	ds_read_b128 v[40:43], v131
	v_fmac_f32_e32 v165, v39, v46
	v_fmac_f32_e32 v164, v39, v47
	ds_read_b128 v[44:47], v132
	v_fmac_f32_e32 v177, v39, v48
	v_fmac_f32_e32 v178, v39, v49
	v_fmac_f32_e32 v176, v39, v50
	v_fmac_f32_e32 v175, v39, v51
	s_waitcnt lgkmcnt(2)
	v_fmac_f32_e32 v174, v39, v52
	v_fmac_f32_e32 v173, v39, v53
	v_fmac_f32_e32 v172, v39, v54
	v_fmac_f32_e32 v171, v39, v55
	s_waitcnt lgkmcnt(1)
	v_fmac_f32_e32 v177, v36, v40
	v_fmac_f32_e32 v178, v36, v41
	v_fmac_f32_e32 v176, v36, v42
	v_fmac_f32_e32 v175, v36, v43
	s_waitcnt lgkmcnt(0)
	v_fmac_f32_e32 v174, v36, v44
	ds_read_b128 v[38:41], v133
	v_fmac_f32_e32 v173, v36, v45
	ds_read_b128 v[42:45], v134
	v_fmac_f32_e32 v172, v36, v46
	v_fmac_f32_e32 v171, v36, v47
	s_waitcnt lgkmcnt(1)
	v_fmac_f32_e32 v170, v36, v38
	v_fmac_f32_e32 v169, v36, v39
	v_fmac_f32_e32 v168, v36, v40
	v_fmac_f32_e32 v167, v36, v41
	s_waitcnt lgkmcnt(0)
	v_fmac_f32_e32 v166, v36, v42
	v_fmac_f32_e32 v163, v36, v43
	ds_read_b128 v[38:41], v135
	ds_read_b128 v[46:49], v136
	v_fmac_f32_e32 v165, v36, v44
	v_fmac_f32_e32 v164, v36, v45
	ds_read_b128 v[42:45], v142
	ds_read_b128 v[50:53], v143
	s_waitcnt lgkmcnt(2)
	v_fmac_f32_e32 v177, v37, v46
	v_fmac_f32_e32 v178, v37, v47
	s_waitcnt lgkmcnt(1)
	v_fmac_f32_e32 v170, v37, v42
	v_fmac_f32_e32 v169, v37, v43
	v_fmac_f32_e32 v168, v37, v44
	v_fmac_f32_e32 v167, v37, v45
	ds_read_b128 v[42:45], v144
	v_fmac_f32_e32 v176, v37, v48
	v_fmac_f32_e32 v175, v37, v49
	s_waitcnt lgkmcnt(1)
	v_fmac_f32_e32 v174, v37, v50
	v_fmac_f32_e32 v173, v37, v51
	v_fmac_f32_e32 v172, v37, v52
	v_fmac_f32_e32 v171, v37, v53
	v_fmac_f32_e32 v166, v37, v38
	v_fmac_f32_e32 v163, v37, v39
	v_fmac_f32_e32 v165, v37, v40
	v_fmac_f32_e32 v164, v37, v41
	ds_read_b128 v[36:39], v145
	s_waitcnt lgkmcnt(1)
	v_fmac_f32_e32 v177, v34, v42
	v_fmac_f32_e32 v178, v34, v43
	ds_read_b128 v[40:43], v146
	v_fmac_f32_e32 v176, v34, v44
	s_waitcnt lgkmcnt(1)
	v_fmac_f32_e32 v174, v34, v36
	v_fmac_f32_e32 v173, v34, v37
	v_fmac_f32_e32 v172, v34, v38
	v_fmac_f32_e32 v171, v34, v39
	ds_read_b128 v[36:39], v147
	v_fmac_f32_e32 v175, v34, v45
	s_waitcnt lgkmcnt(1)
	v_fmac_f32_e32 v170, v34, v40
	v_fmac_f32_e32 v169, v34, v41
	v_fmac_f32_e32 v168, v34, v42
	v_fmac_f32_e32 v167, v34, v43
	ds_read_b128 v[40:43], v148
	ds_read_b128 v[44:47], v149
	s_waitcnt lgkmcnt(2)
	v_fmac_f32_e32 v166, v34, v36
	v_fmac_f32_e32 v163, v34, v37
	v_fmac_f32_e32 v165, v34, v38
	v_fmac_f32_e32 v164, v34, v39
	ds_read_b128 v[36:39], v150
	ds_read_b128 v[48:51], v151
	s_waitcnt lgkmcnt(2)
	v_fmac_f32_e32 v177, v35, v44
	v_fmac_f32_e32 v178, v35, v45
	v_fmac_f32_e32 v176, v35, v46
	v_fmac_f32_e32 v175, v35, v47
	s_waitcnt lgkmcnt(1)
	v_fmac_f32_e32 v168, v35, v38
	v_fmac_f32_e32 v167, v35, v39
	v_fmac_f32_e32 v166, v35, v40
	v_fmac_f32_e32 v163, v35, v41
	ds_read_b128 v[38:41], v152
	ds_read_b128 v[44:47], v157
	s_waitcnt lgkmcnt(2)
	v_fmac_f32_e32 v174, v35, v48
	v_fmac_f32_e32 v173, v35, v49
	v_fmac_f32_e32 v172, v35, v50
	v_fmac_f32_e32 v171, v35, v51
	v_fmac_f32_e32 v170, v35, v36
	v_fmac_f32_e32 v169, v35, v37
	v_fmac_f32_e32 v165, v35, v42
	v_fmac_f32_e32 v164, v35, v43
	ds_read_b128 v[34:37], v153
	s_waitcnt lgkmcnt(2)
	v_mov_b32_e32 v42, v39
	ds_read_b128 v[48:51], v156
	s_waitcnt lgkmcnt(2)
	v_mov_b32_e32 v43, v45
	v_pk_mul_f32 v[56:57], v[32:33], v[42:43]
	v_fmac_f32_e32 v176, v32, v40
	v_fmac_f32_e32 v175, v32, v41
	s_waitcnt lgkmcnt(1)
	v_fmac_f32_e32 v174, v32, v34
	ds_read_b128 v[40:43], v154
	v_fmac_f32_e32 v173, v32, v35
	v_fmac_f32_e32 v172, v32, v36
	v_fmac_f32_e32 v171, v32, v37
	ds_read_b128 v[34:37], v155
	v_mov_b32_e32 v39, v44
	v_pk_mul_f32 v[38:39], v[32:33], v[38:39]
	s_waitcnt lgkmcnt(1)
	v_fmac_f32_e32 v170, v32, v40
	v_fmac_f32_e32 v169, v32, v41
	v_fmac_f32_e32 v168, v32, v42
	v_fmac_f32_e32 v167, v32, v43
	s_waitcnt lgkmcnt(0)
	v_fmac_f32_e32 v166, v32, v34
	v_fmac_f32_e32 v163, v32, v35
	v_fmac_f32_e32 v165, v32, v36
	v_fmac_f32_e32 v164, v32, v37
	v_add_f32_e32 v32, v177, v38
	v_add_f32_e32 v32, v32, v39
	s_nop 1
	v_mov_b32_dpp v38, v32 quad_perm:[1,0,3,2] row_mask:0xf bank_mask:0xf
	v_add_f32_e32 v45, v178, v56
	v_add_f32_e32 v39, v45, v57
	s_nop 1
	v_mov_b32_dpp v44, v39 quad_perm:[1,0,3,2] row_mask:0xf bank_mask:0xf
	v_mov_b32_e32 v34, s7
	s_waitcnt lgkmcnt(0)
	v_add_f32_e32 v32, v32, v38
	s_nop 1
	v_mov_b32_dpp v38, v32 quad_perm:[2,3,0,1] row_mask:0xf bank_mask:0xf
	ds_read_b128 v[34:37], v34
	ds_read_b128 v[40:43], v158
	ds_read_b128 v[52:55], v159
	s_waitcnt lgkmcnt(3)
	v_add_f32_e32 v39, v39, v44
	v_fmac_f32_e32 v176, v33, v46
	v_fmac_f32_e32 v175, v33, v47
	s_waitcnt lgkmcnt(3)
	v_add_f32_e32 v32, v32, v38
	s_nop 1
	v_mov_b32_dpp v38, v32 row_half_mirror row_mask:0xf bank_mask:0xf
	s_waitcnt lgkmcnt(1)
	v_fmac_f32_e32 v170, v33, v40
	s_nop 1
	v_mov_b32_dpp v40, v39 quad_perm:[2,3,0,1] row_mask:0xf bank_mask:0xf
	s_waitcnt lgkmcnt(0)
	v_fmac_f32_e32 v174, v33, v52
	v_fmac_f32_e32 v173, v33, v53
	s_waitcnt lgkmcnt(0)
	v_add_f32_e32 v32, v32, v38
	s_nop 1
	v_mov_b32_dpp v38, v32 row_mirror row_mask:0xf bank_mask:0xf
	s_waitcnt lgkmcnt(0)
	v_add_f32_e32 v39, v39, v40
	s_nop 1
	v_mov_b32_dpp v40, v39 row_half_mirror row_mask:0xf bank_mask:0xf
	v_fmac_f32_e32 v172, v33, v54
	v_fmac_f32_e32 v171, v33, v55
	s_waitcnt lgkmcnt(0)
	v_add_f32_e32 v32, v32, v38
	ds_bpermute_b32 v38, v161, v32
	s_waitcnt lgkmcnt(1)
	v_add_f32_e32 v39, v39, v40
	s_nop 1
	v_mov_b32_dpp v40, v39 row_mirror row_mask:0xf bank_mask:0xf
	v_fmac_f32_e32 v169, v33, v41
	v_fmac_f32_e32 v168, v33, v42
	s_waitcnt lgkmcnt(0)
	v_add_f32_e32 v32, v32, v38
	ds_bpermute_b32 v38, v162, v32
	v_fmac_f32_e32 v167, v33, v43
	v_fmac_f32_e32 v166, v33, v48
	v_fmac_f32_e32 v163, v33, v49
	v_fmac_f32_e32 v165, v33, v50
	v_fmac_f32_e32 v164, v33, v51
	s_waitcnt lgkmcnt(1)
	v_add_f32_e32 v33, v39, v40
	ds_bpermute_b32 v39, v161, v33
	s_waitcnt lgkmcnt(1)
	v_add_f32_e32 v32, v32, v38
	s_nop 1
	v_mov_b32_dpp v38, v176 quad_perm:[1,0,3,2] row_mask:0xf bank_mask:0xf
	v_mul_f32_e32 v32, 0xbfb8aa3b, v32
	v_exp_f32_e32 v32, v32
	s_waitcnt lgkmcnt(0)
	v_add_f32_e32 v33, v33, v39
	ds_bpermute_b32 v39, v162, v33
	s_waitcnt lgkmcnt(1)
	v_add_f32_e32 v38, v176, v38
	s_nop 1
	v_mov_b32_dpp v40, v38 quad_perm:[2,3,0,1] row_mask:0xf bank_mask:0xf
	s_nop 1
	v_mov_b32_dpp v41, v175 quad_perm:[1,0,3,2] row_mask:0xf bank_mask:0xf
	v_add_f32_e32 v32, 1.0, v32
	v_rcp_f32_e32 v52, v32
	s_waitcnt lgkmcnt(0)
	v_add_f32_e32 v32, v33, v39
	s_waitcnt lgkmcnt(0)
	v_add_f32_e32 v33, v38, v40
	s_waitcnt lgkmcnt(0)
	v_add_f32_e32 v39, v175, v41
	s_nop 1
	v_mov_b32_dpp v38, v33 row_half_mirror row_mask:0xf bank_mask:0xf
	s_nop 1
	v_mov_b32_dpp v40, v39 quad_perm:[2,3,0,1] row_mask:0xf bank_mask:0xf
	v_mul_f32_e32 v32, 0xbfb8aa3b, v32
	v_exp_f32_e32 v32, v32
	v_add_f32_e32 v138, v34, v52
	s_waitcnt lgkmcnt(0)
	v_add_f32_e32 v33, v33, v38
	s_waitcnt lgkmcnt(0)
	v_add_f32_e32 v39, v39, v40
	s_nop 1
	v_mov_b32_dpp v38, v33 row_mirror row_mask:0xf bank_mask:0xf
	s_nop 1
	v_mov_b32_dpp v40, v39 row_half_mirror row_mask:0xf bank_mask:0xf
	v_add_f32_e32 v32, 1.0, v32
	v_rcp_f32_e32 v46, v32
	s_nop 1
	v_mov_b32_dpp v34, v174 quad_perm:[1,0,3,2] row_mask:0xf bank_mask:0xf
	s_waitcnt lgkmcnt(0)
	v_add_f32_e32 v32, v33, v38
	s_waitcnt lgkmcnt(0)
	v_add_f32_e32 v42, v39, v40
	ds_bpermute_b32 v33, v161, v32
	s_nop 1
	v_mov_b32_dpp v43, v42 row_mirror row_mask:0xf bank_mask:0xf
	s_waitcnt lgkmcnt(1)
	v_add_f32_e32 v34, v174, v34
	v_add_f32_e32 v47, v35, v46
	s_nop 1
	v_mov_b32_dpp v35, v34 quad_perm:[2,3,0,1] row_mask:0xf bank_mask:0xf
	s_waitcnt lgkmcnt(0)
	v_add_f32_e32 v180, v32, v33
	s_waitcnt lgkmcnt(0)
	v_add_f32_e32 v32, v42, v43
	ds_bpermute_b32 v33, v161, v32
	s_nop 1
	v_mov_b32_dpp v42, v173 quad_perm:[1,0,3,2] row_mask:0xf bank_mask:0xf
	s_nop 1
	v_mov_b32_dpp v139, v163 quad_perm:[1,0,3,2] row_mask:0xf bank_mask:0xf
	v_mov_b32_e32 v38, s86
	ds_read_b128 v[38:41], v38
	s_waitcnt lgkmcnt(1)
	v_add_f32_e32 v57, v32, v33
	s_nop 1
	v_mov_b32_dpp v32, v172 quad_perm:[1,0,3,2] row_mask:0xf bank_mask:0xf
	v_add_f32_e32 v33, v34, v35
	s_waitcnt lgkmcnt(1)
	v_add_f32_e32 v35, v173, v42
	s_nop 1
	v_mov_b32_dpp v34, v33 row_half_mirror row_mask:0xf bank_mask:0xf
	s_nop 1
	v_mov_b32_dpp v42, v35 quad_perm:[2,3,0,1] row_mask:0xf bank_mask:0xf
	s_waitcnt lgkmcnt(0)
	v_add_f32_e32 v32, v172, v32
	s_nop 1
	v_mov_b32_dpp v43, v32 quad_perm:[2,3,0,1] row_mask:0xf bank_mask:0xf
	v_add_f32_e32 v139, v163, v139
	s_waitcnt lgkmcnt(0)
	v_add_f32_e32 v33, v33, v34
	s_waitcnt lgkmcnt(0)
	v_add_f32_e32 v35, v35, v42
	s_nop 1
	v_mov_b32_dpp v34, v33 row_mirror row_mask:0xf bank_mask:0xf
	s_nop 1
	v_mov_b32_dpp v42, v35 row_half_mirror row_mask:0xf bank_mask:0xf
	s_waitcnt lgkmcnt(0)
	v_add_f32_e32 v32, v32, v43
	s_nop 1
	v_mov_b32_dpp v43, v32 row_half_mirror row_mask:0xf bank_mask:0xf
	s_nop 1
	v_mov_b32_dpp v163, v139 quad_perm:[2,3,0,1] row_mask:0xf bank_mask:0xf
	s_waitcnt lgkmcnt(0)
	v_add_f32_e32 v33, v33, v34
	s_waitcnt lgkmcnt(0)
	v_add_f32_e32 v35, v35, v42
	ds_bpermute_b32 v34, v161, v33
	s_nop 1
	v_mov_b32_dpp v42, v35 row_mirror row_mask:0xf bank_mask:0xf
	s_waitcnt lgkmcnt(1)
	v_add_f32_e32 v32, v32, v43
	s_nop 1
	v_mov_b32_dpp v43, v32 row_mirror row_mask:0xf bank_mask:0xf
	s_waitcnt lgkmcnt(1)
	v_add_f32_e32 v139, v139, v163
	s_waitcnt lgkmcnt(0)
	v_add_f32_e32 v54, v33, v34
	s_waitcnt lgkmcnt(0)
	v_add_f32_e32 v33, v35, v42
	ds_bpermute_b32 v34, v161, v33
	s_waitcnt lgkmcnt(1)
	v_add_f32_e32 v32, v32, v43
	s_nop 1
	v_mov_b32_dpp v42, v171 quad_perm:[1,0,3,2] row_mask:0xf bank_mask:0xf
	ds_bpermute_b32 v35, v161, v32
	s_nop 1
	v_mov_b32_dpp v163, v139 row_half_mirror row_mask:0xf bank_mask:0xf
	s_waitcnt lgkmcnt(1)
	v_add_f32_e32 v58, v33, v34
	ds_bpermute_b32 v181, v162, v180
	s_waitcnt lgkmcnt(2)
	v_add_f32_e32 v33, v171, v42
	s_waitcnt lgkmcnt(1)
	v_add_f32_e32 v55, v32, v35
	s_nop 1
	v_mov_b32_dpp v34, v33 quad_perm:[2,3,0,1] row_mask:0xf bank_mask:0xf
	s_nop 1
	v_mov_b32_dpp v35, v169 quad_perm:[1,0,3,2] row_mask:0xf bank_mask:0xf
	s_nop 1
	v_mov_b32_dpp v32, v170 quad_perm:[1,0,3,2] row_mask:0xf bank_mask:0xf
	ds_bpermute_b32 v172, v162, v57
	ds_bpermute_b32 v179, v162, v54
	s_waitcnt lgkmcnt(2)
	v_add_f32_e32 v33, v33, v34
	s_waitcnt lgkmcnt(2)
	v_add_f32_e32 v35, v169, v35
	s_nop 1
	v_mov_b32_dpp v34, v33 row_half_mirror row_mask:0xf bank_mask:0xf
	s_nop 1
	v_mov_b32_dpp v43, v35 quad_perm:[2,3,0,1] row_mask:0xf bank_mask:0xf
	s_waitcnt lgkmcnt(2)
	v_add_f32_e32 v32, v170, v32
	s_nop 1
	v_mov_b32_dpp v42, v32 quad_perm:[2,3,0,1] row_mask:0xf bank_mask:0xf
	ds_bpermute_b32 v178, v162, v58
	s_waitcnt lgkmcnt(1)
	v_add_f32_e32 v33, v33, v34
	s_waitcnt lgkmcnt(1)
	v_add_f32_e32 v35, v35, v43
	s_nop 1
	v_mov_b32_dpp v34, v33 row_mirror row_mask:0xf bank_mask:0xf
	s_nop 1
	v_mov_b32_dpp v43, v35 row_half_mirror row_mask:0xf bank_mask:0xf
	s_waitcnt lgkmcnt(1)
	v_add_f32_e32 v32, v32, v42
	s_nop 1
	v_mov_b32_dpp v42, v32 row_half_mirror row_mask:0xf bank_mask:0xf
	ds_bpermute_b32 v56, v162, v55
	s_waitcnt lgkmcnt(1)
	v_add_f32_e32 v33, v33, v34
	s_waitcnt lgkmcnt(1)
	v_add_f32_e32 v35, v35, v43
	ds_bpermute_b32 v34, v161, v33
	s_nop 1
	v_mov_b32_dpp v43, v35 row_mirror row_mask:0xf bank_mask:0xf
	s_waitcnt lgkmcnt(2)
	v_add_f32_e32 v32, v32, v42
	s_nop 1
	v_mov_b32_dpp v42, v32 row_mirror row_mask:0xf bank_mask:0xf
	v_cmp_lt_f32_e64 s[44:45], s17, v138
	s_waitcnt lgkmcnt(0)
	v_add_f32_e32 v59, v33, v34
	s_waitcnt lgkmcnt(0)
	v_add_f32_e32 v33, v35, v43
	ds_bpermute_b32 v34, v161, v33
	s_waitcnt lgkmcnt(1)
	v_add_f32_e32 v32, v32, v42
	s_nop 1
	v_mov_b32_dpp v35, v168 quad_perm:[1,0,3,2] row_mask:0xf bank_mask:0xf
	ds_bpermute_b32 v42, v161, v32
	ds_bpermute_b32 v177, v162, v59
	s_waitcnt lgkmcnt(2)
	v_add_f32_e32 v49, v33, v34
	s_nop 1
	v_mov_b32_dpp v33, v167 quad_perm:[1,0,3,2] row_mask:0xf bank_mask:0xf
	s_nop 1
	v_mov_b32_dpp v34, v166 quad_perm:[1,0,3,2] row_mask:0xf bank_mask:0xf
	s_waitcnt lgkmcnt(2)
	v_add_f32_e32 v35, v168, v35
	s_waitcnt lgkmcnt(1)
	v_add_f32_e32 v48, v32, v42
	s_nop 1
	v_mov_b32_dpp v42, v35 quad_perm:[2,3,0,1] row_mask:0xf bank_mask:0xf
	s_waitcnt lgkmcnt(0)
	v_add_f32_e32 v33, v167, v33
	s_nop 1
	v_mov_b32_dpp v167, v165 quad_perm:[1,0,3,2] row_mask:0xf bank_mask:0xf
	s_nop 1
	v_mov_b32_dpp v60, v164 quad_perm:[1,0,3,2] row_mask:0xf bank_mask:0xf
	s_waitcnt lgkmcnt(0)
	v_add_f32_e32 v34, v166, v34
	s_nop 1
	v_mov_b32_dpp v43, v33 quad_perm:[2,3,0,1] row_mask:0xf bank_mask:0xf
	s_nop 1
	v_mov_b32_dpp v44, v34 quad_perm:[2,3,0,1] row_mask:0xf bank_mask:0xf
	s_waitcnt lgkmcnt(0)
	v_add_f32_e32 v165, v165, v167
	s_waitcnt lgkmcnt(0)
	v_add_f32_e32 v60, v164, v60
	s_nop 1
	v_mov_b32_dpp v167, v165 quad_perm:[2,3,0,1] row_mask:0xf bank_mask:0xf
	s_nop 1
	v_mov_b32_dpp v61, v60 quad_perm:[2,3,0,1] row_mask:0xf bank_mask:0xf
	v_add_f32_e32 v35, v35, v42
	s_waitcnt lgkmcnt(0)
	v_add_f32_e32 v33, v33, v43
	s_waitcnt lgkmcnt(0)
	v_add_f32_e32 v34, v34, v44
	s_waitcnt lgkmcnt(0)
	v_add_f32_e32 v164, v165, v167
	s_waitcnt lgkmcnt(0)
	v_add_f32_e32 v60, v60, v61
	s_nop 1
	v_mov_b32_dpp v42, v35 row_half_mirror row_mask:0xf bank_mask:0xf
	s_nop 1
	v_mov_b32_dpp v43, v33 row_half_mirror row_mask:0xf bank_mask:0xf
	s_nop 1
	v_mov_b32_dpp v44, v34 row_half_mirror row_mask:0xf bank_mask:0xf
	s_nop 1
	v_mov_b32_dpp v165, v164 row_half_mirror row_mask:0xf bank_mask:0xf
	s_nop 1
	v_mov_b32_dpp v61, v60 row_half_mirror row_mask:0xf bank_mask:0xf
	s_waitcnt lgkmcnt(0)
	v_add_f32_e32 v35, v35, v42
	s_waitcnt lgkmcnt(0)
	v_add_f32_e32 v33, v33, v43
	s_waitcnt lgkmcnt(0)
	v_add_f32_e32 v34, v34, v44
	v_add_f32_e32 v62, v139, v163
	s_waitcnt lgkmcnt(0)
	v_add_f32_e32 v163, v164, v165
	s_waitcnt lgkmcnt(0)
	v_add_f32_e32 v60, v60, v61
	s_nop 1
	v_mov_b32_dpp v42, v35 row_mirror row_mask:0xf bank_mask:0xf
	s_nop 1
	v_mov_b32_dpp v43, v33 row_mirror row_mask:0xf bank_mask:0xf
	s_nop 1
	v_mov_b32_dpp v44, v34 row_mirror row_mask:0xf bank_mask:0xf
	s_nop 1
	v_mov_b32_dpp v139, v62 row_mirror row_mask:0xf bank_mask:0xf
	s_nop 1
	v_mov_b32_dpp v164, v163 row_mirror row_mask:0xf bank_mask:0xf
	s_nop 1
	v_mov_b32_dpp v61, v60 row_mirror row_mask:0xf bank_mask:0xf
	s_waitcnt lgkmcnt(0)
	v_add_f32_e32 v35, v35, v42
	s_waitcnt lgkmcnt(0)
	v_add_f32_e32 v33, v33, v43
	s_waitcnt lgkmcnt(0)
	v_add_f32_e32 v34, v34, v44
	s_waitcnt lgkmcnt(0)
	v_add_f32_e32 v62, v62, v139
	s_waitcnt lgkmcnt(0)
	v_add_f32_e32 v139, v163, v164
	s_waitcnt lgkmcnt(0)
	v_add_f32_e32 v60, v60, v61
	ds_bpermute_b32 v42, v161, v35
	ds_bpermute_b32 v43, v161, v33
	ds_bpermute_b32 v44, v161, v34
	ds_bpermute_b32 v63, v161, v62
	ds_bpermute_b32 v163, v161, v139
	ds_bpermute_b32 v61, v161, v60
	v_mov_b32_e32 v32, s81
	s_waitcnt lgkmcnt(5)
	v_add_f32_e32 v175, v35, v42
	s_waitcnt lgkmcnt(4)
	v_add_f32_e32 v51, v33, v43
	s_waitcnt lgkmcnt(3)
	v_add_f32_e32 v166, v34, v44
	v_mov_b32_e32 v33, s23
	s_waitcnt lgkmcnt(2)
	v_add_f32_e32 v173, v62, v63
	s_waitcnt lgkmcnt(1)
	v_add_f32_e32 v169, v139, v163
	s_waitcnt lgkmcnt(0)
	v_add_f32_e32 v164, v60, v61
	ds_bpermute_b32 v50, v162, v48
	ds_bpermute_b32 v53, v162, v49
	ds_bpermute_b32 v176, v162, v175
	ds_bpermute_b32 v171, v162, v51
	ds_bpermute_b32 v168, v162, v166
	ds_read_b128 v[42:45], v32
	ds_read_b128 v[32:35], v33
	ds_bpermute_b32 v174, v162, v173
	ds_bpermute_b32 v170, v162, v169
	ds_bpermute_b32 v165, v162, v164
	v_max_f32_e32 v161, 0xf149f2ca, v138
	v_cmp_ngt_f32_e64 s[42:43], v47, v161
	v_mov_b32_e32 v60, v47
	v_mov_b32_e32 v61, v161
	s_and_saveexec_b64 s[12:13], s[42:43]
	s_cbranch_execz .LBB0_1241
	v_mov_b32_e32 v61, 0xf149f2ca
	v_cmp_gt_f32_e32 vcc, v47, v61
	s_and_saveexec_b64 s[14:15], vcc
	v_mov_b32_e32 v61, v47
	s_or_b64 exec, exec, s[14:15]
	v_mov_b32_e32 v60, v161
